# speedup vs baseline: 1.0005x; 1.0005x over previous
.LBB4_35:
	s_or_b64 exec, exec, s[16:17]
	s_waitcnt vmcnt(0)
	ds_write_b128 v72, v[18:21] offset:52224
	v_and_b32_e32 v19, 16, v0
	v_add_u32_e32 v20, 14, v0
	s_load_dwordx2 s[6:7], s[0:1], 0x40
	v_and_b32_e32 v20, 15, v20
	v_cmp_eq_u32_e64 s[0:1], 0, v19
	v_or_b32_e32 v18, v105, v73
	v_mad_u32_u24 v80, v101, 6, 4
	v_cndmask_b32_e64 v19, v20, v98, s[0:1]
	v_mad_u32_u24 v21, v18, 18, v19
	v_lshl_or_b32 v18, v18, 4, v19
	s_movk_i32 s0, 0x50
	v_mov_b32_e32 v19, 0xfc00
	v_mad_u32_u24 v78, v18, s0, v19
	v_or_b32_e32 v18, v106, v98
	v_mul_u32_u24_e32 v22, 6, v101
	v_or_b32_e32 v81, 0xffffff60, v98
	v_mad_u32_u24 v18, v18, s0, v19
	s_movk_i32 s0, 0x60
	v_lshlrev_b32_e32 v95, 11, v80
	v_lshlrev_b32_e32 v80, 4, v80
	v_add_u32_e32 v83, 19, v98
	v_mul_u32_u24_e32 v24, 0x60, v101
	v_mad_u32_u24 v25, v101, s0, v81
	v_mov_b32_e32 v27, 0xffffff5d
	s_movk_i32 s0, 0x6c
	v_or_b32_e32 v22, 1, v22
	v_add_u32_e32 v90, v80, v81
	v_or_b32_e32 v91, v80, v98
	v_mad_u32_u24 v80, v101, 6, 5
	v_or_b32_e32 v24, v24, v98
	v_mad_i32_i24 v28, v25, 18, v27
	v_mad_u32_u24 v29, v101, s0, v83
	v_lshlrev_b32_e32 v31, 4, v22
	v_lshlrev_b32_e32 v97, 11, v80
	v_lshlrev_b32_e32 v80, 4, v80
	v_cmp_gt_u32_e64 s[0:1], 20, v25
	v_or_b32_e32 v23, v104, v98
	v_mul_i32_i24_e32 v26, 18, v25
	v_add_u32_e32 v32, v31, v81
	v_add_u32_e32 v104, v80, v81
	v_or_b32_e32 v105, v80, v98
	v_mul_u32_u24_e32 v80, 0x90, v21
	v_cndmask_b32_e64 v21, v24, v28, s[0:1]
	v_cmp_gt_i32_e64 s[0:1], 10, v25
	v_or_b32_e32 v31, v31, v98
	v_mad_i32_i24 v34, v32, 18, v27
	v_mad_u32_u24 v35, v101, 6, 2
	v_cndmask_b32_e64 v21, v21, v26, s[0:1]
	v_cmp_gt_u32_e64 s[0:1], 20, v32
	v_mul_i32_i24_e32 v33, 18, v32
	v_lshlrev_b32_e32 v36, 11, v35
	v_lshlrev_b32_e32 v35, 4, v35
	v_cndmask_b32_e64 v24, v31, v34, s[0:1]
	v_cmp_gt_i32_e64 s[0:1], 10, v32
	v_readfirstlane_b32 s10, v99
	v_lshlrev_b32_e32 v30, 11, v22
	v_mad_u32_u24 v22, v22, 18, v83
	v_add_u32_e32 v37, v35, v81
	v_mad_u32_u24 v77, v101, 6, 3
	v_cndmask_b32_e64 v24, v24, v33, s[0:1]
	s_mul_i32 s8, s10, 9
	s_lshl_b32 s25, s10, 4
	v_or_b32_e32 v35, v35, v98
	v_mad_i32_i24 v73, v37, 18, v27
	v_add_u32_e32 v76, 18, v22
	v_lshlrev_b32_e32 v93, 11, v77
	v_lshlrev_b32_e32 v77, 4, v77
	v_add_u32_e32 v89, 36, v22
	v_add_u32_e32 v96, 54, v22
	v_add_u32_e32 v107, 0x48, v22
	s_movk_i32 s10, 0x90
	v_cndmask_b32_e32 v21, v21, v29, vcc
	v_cndmask_b32_e32 v22, v24, v22, vcc
	v_cmp_gt_u32_e32 vcc, 20, v37
	v_add_u32_e32 v39, 0xcc00, v72
	v_mul_i32_i24_e32 v72, 18, v37
	v_add_u32_e32 v85, v77, v81
	v_mul_lo_u32 v24, v22, s10
	v_cndmask_b32_e32 v22, v35, v73, vcc
	v_cmp_gt_i32_e32 vcc, 10, v37
	v_or_b32_e32 v77, v77, v98
	v_mad_i32_i24 v88, v85, 18, v27
	v_cndmask_b32_e32 v22, v22, v72, vcc
	v_cmp_gt_u32_e32 vcc, 20, v85
	v_mul_i32_i24_e32 v87, 18, v85
	v_mad_i32_i24 v94, v90, 18, v27
	v_cndmask_b32_e32 v25, v77, v88, vcc
	v_cmp_gt_i32_e32 vcc, 10, v85
	v_mul_i32_i24_e32 v92, 18, v90
	v_mad_i32_i24 v27, v104, 18, v27
	v_cndmask_b32_e32 v25, v25, v87, vcc
	v_cmp_gt_u32_e32 vcc, 20, v90
	v_mul_i32_i24_e32 v106, 18, v104
	v_add_u32_e32 v82, 1, v98
	v_cndmask_b32_e32 v26, v91, v94, vcc
	v_cmp_gt_i32_e32 vcc, 10, v90
	v_add_u32_e32 v79, 0xa3, v98
	v_lshrrev_b32_e32 v85, 7, v0
	v_cndmask_b32_e32 v26, v26, v92, vcc
	v_cmp_gt_u32_e32 vcc, 20, v104
	s_movk_i32 s0, 0x70
	v_mul_u32_u24_e32 v38, 0xc0, v23
	v_cndmask_b32_e32 v27, v105, v27, vcc
	v_cmp_gt_i32_e32 vcc, 10, v104
	v_mov_b32_e32 v23, 0
	s_waitcnt lgkmcnt(0)
	s_barrier
	v_cndmask_b32_e64 v26, v26, v96, s[4:5]
	v_cndmask_b32_e32 v27, v27, v106, vcc
	v_cmp_ne_u32_e32 vcc, 0, v101
	v_cndmask_b32_e64 v27, v27, v107, s[4:5]
	s_ashr_i32 s9, s8, 31
	v_cndmask_b32_e32 v22, v22, v82, vcc
	v_cndmask_b32_e64 v22, v22, v76, s[4:5]
	v_mul_lo_u32 v28, v22, s10
	v_cndmask_b32_e32 v22, v25, v79, vcc
	v_cndmask_b32_e64 v22, v22, v89, s[4:5]
	v_mul_lo_u32 v25, v22, s10
	v_lshlrev_b32_e32 v22, 7, v98
	v_lshl_or_b32 v22, v85, 11, v22
	v_and_or_b32 v22, v0, s0, v22
	s_mov_b64 s[0:1], 0xc900
	v_or_b32_e32 v75, 0xcc00, v102
	v_or_b32_e32 v84, 0x6c00, v102
	v_lshl_or_b32 v20, v99, 5, v103
	v_mul_u32_u24_e32 v19, 0x3000, v101
	v_mul_lo_u32 v21, v21, s10
	v_mul_lo_u32 v26, v26, s10
	v_mul_lo_u32 v27, v27, s10
	v_lshl_add_u64 v[72:73], v[22:23], 0, s[0:1]
	v_lshl_or_b32 v22, v38, 1, v74
	s_mov_b64 s[0:1], 0x18400
	v_lshl_add_u32 v86, v99, 11, v75
	s_mov_b32 s23, 5
	v_lshl_add_u64 v[76:77], v[22:23], 0, s[0:1]
	s_lshl_b64 s[0:1], s[8:9], 4
	v_add_u32_e32 v87, v84, v19
	v_add_u32_e32 v88, v20, v21
	v_add_u32_e32 v89, v84, v30
	v_add_u32_e32 v90, v20, v24
	v_add_u32_e32 v91, v84, v36
	v_add_u32_e32 v92, v20, v28
	v_add_u32_e32 v93, v84, v93
	v_add_u32_e32 v94, v20, v25
	v_add_u32_e32 v95, v84, v95
	v_add_u32_e32 v96, v20, v26
	v_add_u32_e32 v97, v84, v97
	v_add_u32_e32 v101, v20, v27
	s_mov_b32 s31, 0x3e6d3387
	s_mov_b32 s22, 0xbf3a00e3
	s_mov_b32 s24, 0x3f07dc22
	s_mov_b32 s26, 0x3f35f0e3
	s_mov_b32 s28, 0xbe11a98e
	s_mov_b32 s30, 0x3e027906
	s_mov_b64 s[34:35], 0x2000
	v_mov_b32_e32 v104, 1.0
	v_add_u32_e32 v74, v18, v74
	v_readfirstlane_b32 s100, v85
	s_cmp_eq_u32 s100, 3
	s_cbranch_scc1 .Lp1_nt3
	s_mul_i32 s101, s100, 54
	s_add_i32 s101, s101, 19
	v_add_u32_e32 v88, s101, v98
	v_add_u32_e32 v90, 18, v88
	v_add_u32_e32 v92, 36, v88
	s_cmp_eq_u32 s100, 2
	s_cbranch_scc0 .Lp1_smap_done
	v_add_u32_e32 v92, 1, v98
	s_branch .Lp1_smap_done

.LBB4_39:
	s_or_b64 exec, exec, s[32:33]
	s_add_u32 s16, s20, s0
	s_addc_u32 s17, s21, s1
	s_load_dwordx8 s[36:43], s[16:17], 0x16900
	s_load_dwordx8 s[44:51], s[16:17], 0x16920
	s_load_dwordx8 s[52:59], s[16:17], 0x16940
	s_load_dwordx8 s[60:67], s[16:17], 0x16960
	s_load_dwordx4 s[68:71], s[16:17], 0x16980
	s_load_dwordx8 s[72:79], s[16:17], 0x16b40
	s_load_dwordx8 s[80:87], s[16:17], 0x16b60
	s_load_dwordx8 s[88:95], s[16:17], 0x16b80
	s_load_dwordx4 s[96:99], s[16:17], 0x16ba0
	s_load_dwordx8 s[8:15], s[16:17], 0x16bb0
	s_setprio 1
	ds_read_b128 v[26:29], v86
	ds_read_b128 v[30:33], v86 offset:1024
	ds_read_b128 v[106:109], v86 offset:2048
	ds_read_b128 v[110:113], v86 offset:3072
	s_waitcnt lgkmcnt(2)
	v_mfma_f32_16x16x32_f16 v[34:37], v[26:29], v[40:43], 0
	v_mfma_f32_16x16x32_f16 v[114:117], v[26:29], v[48:51], 0
	v_mfma_f32_16x16x32_f16 v[118:121], v[26:29], v[56:59], 0
	v_mfma_f32_16x16x32_f16 v[34:37], v[30:33], v[44:47], v[34:37]
	v_mfma_f32_16x16x32_f16 v[114:117], v[30:33], v[52:55], v[114:117]
	v_mfma_f32_16x16x32_f16 v[118:121], v[30:33], v[60:63], v[118:121]
	s_waitcnt lgkmcnt(0)
	v_mfma_f32_16x16x32_f16 v[122:125], v[106:109], v[40:43], 0
	v_mfma_f32_16x16x32_f16 v[122:125], v[110:113], v[44:47], v[122:125]
	s_nop 2
	v_cvt_pk_f16_f32 v34, v34, v35
	v_cvt_pk_f16_f32 v35, v36, v37
	ds_write_b64 v88, v[34:35]
	v_cvt_pk_f16_f32 v114, v114, v115
	v_cvt_pk_f16_f32 v115, v116, v117
	ds_write_b64 v90, v[114:115]
	v_cvt_pk_f16_f32 v118, v118, v119
	v_cvt_pk_f16_f32 v119, v120, v121
	ds_write_b64 v92, v[118:119]
	v_mfma_f32_16x16x32_f16 v[34:37], v[106:109], v[48:51], 0
	v_mfma_f32_16x16x32_f16 v[114:117], v[106:109], v[56:59], 0
	v_mfma_f32_16x16x32_f16 v[34:37], v[110:113], v[52:55], v[34:37]
	v_mfma_f32_16x16x32_f16 v[114:117], v[110:113], v[60:63], v[114:117]
	v_cvt_pk_f16_f32 v122, v122, v123
	v_cvt_pk_f16_f32 v123, v124, v125
	ds_write_b64 v88, v[122:123] offset:32
	s_nop 3
	v_cvt_pk_f16_f32 v34, v34, v35
	v_cvt_pk_f16_f32 v35, v36, v37
	ds_write_b64 v90, v[34:35] offset:32
	v_cvt_pk_f16_f32 v114, v114, v115
	v_cvt_pk_f16_f32 v115, v116, v117
	ds_write_b64 v92, v[114:115] offset:32
	s_setprio 0
	s_waitcnt lgkmcnt(0)
	s_barrier
	v_add_u32_e32 v105, s25, v80
	ds_read_b128 v[30:33], v105
	ds_read_b128 v[34:37], v105 offset:64
	ds_read_b128 v[106:109], v105 offset:144
	ds_read_b128 v[110:113], v105 offset:208
	ds_read_b128 v[114:117], v105 offset:288
	ds_read_b128 v[122:125], v105 offset:352
	s_waitcnt lgkmcnt(4)
	v_pk_fma_f16 v118, v30, s36, 0
	v_pk_fma_f16 v119, v31, s37, 0
	v_pk_fma_f16 v120, v32, s38, 0
	v_pk_fma_f16 v121, v33, s39, 0
	v_pk_fma_f16 v26, v34, s72, 0
	v_pk_fma_f16 v27, v35, s73, 0
	v_pk_fma_f16 v28, v36, s74, 0
	v_pk_fma_f16 v29, v37, s75, 0
	ds_read_b128 v[30:33], v105 offset:2592
	ds_read_b128 v[34:37], v105 offset:2656
	s_waitcnt lgkmcnt(4)
	v_pk_fma_f16 v118, v106, s40, v118
	v_pk_fma_f16 v119, v107, s41, v119
	v_pk_fma_f16 v120, v108, s42, v120
	v_pk_fma_f16 v121, v109, s43, v121
	v_pk_fma_f16 v26, v110, s76, v26
	v_pk_fma_f16 v27, v111, s77, v27
	v_pk_fma_f16 v28, v112, s78, v28
	v_pk_fma_f16 v29, v113, s79, v29
	ds_read_b128 v[106:109], v105 offset:2736
	ds_read_b128 v[110:113], v105 offset:2800
	s_waitcnt lgkmcnt(4)
	v_pk_fma_f16 v118, v114, s44, v118
	v_pk_fma_f16 v119, v115, s45, v119
	v_pk_fma_f16 v120, v116, s46, v120
	v_pk_fma_f16 v121, v117, s47, v121
	v_pk_fma_f16 v26, v122, s80, v26
	v_pk_fma_f16 v27, v123, s81, v27
	v_pk_fma_f16 v28, v124, s82, v28
	v_pk_fma_f16 v29, v125, s83, v29
	ds_read_b128 v[114:117], v105 offset:2880
	ds_read_b128 v[122:125], v105 offset:2944
	s_waitcnt lgkmcnt(4)
	v_pk_fma_f16 v118, v30, s48, v118
	v_pk_fma_f16 v119, v31, s49, v119
	v_pk_fma_f16 v120, v32, s50, v120
	v_pk_fma_f16 v121, v33, s51, v121
	v_pk_fma_f16 v26, v34, s84, v26
	v_pk_fma_f16 v27, v35, s85, v27
	v_pk_fma_f16 v28, v36, s86, v28
	v_pk_fma_f16 v29, v37, s87, v29
	ds_read_b128 v[30:33], v105 offset:5184
	ds_read_b128 v[34:37], v105 offset:5248
	s_waitcnt lgkmcnt(4)
	v_pk_fma_f16 v118, v106, s52, v118
	v_pk_fma_f16 v119, v107, s53, v119
	v_pk_fma_f16 v120, v108, s54, v120
	v_pk_fma_f16 v121, v109, s55, v121
	v_pk_fma_f16 v26, v110, s88, v26
	v_pk_fma_f16 v27, v111, s89, v27
	v_pk_fma_f16 v28, v112, s90, v28
	v_pk_fma_f16 v29, v113, s91, v29
	ds_read_b128 v[106:109], v105 offset:5328
	ds_read_b128 v[110:113], v105 offset:5392
	s_waitcnt lgkmcnt(4)
	v_pk_fma_f16 v118, v114, s56, v118
	v_pk_fma_f16 v119, v115, s57, v119
	v_pk_fma_f16 v120, v116, s58, v120
	v_pk_fma_f16 v121, v117, s59, v121
	v_pk_fma_f16 v26, v122, s92, v26
	v_pk_fma_f16 v27, v123, s93, v27
	v_pk_fma_f16 v28, v124, s94, v28
	v_pk_fma_f16 v29, v125, s95, v29
	ds_read_b128 v[114:117], v105 offset:5472
	ds_read_b128 v[122:125], v105 offset:5536
	s_waitcnt lgkmcnt(4)
	v_pk_fma_f16 v118, v30, s60, v118
	v_pk_fma_f16 v119, v31, s61, v119
	v_pk_fma_f16 v120, v32, s62, v120
	v_pk_fma_f16 v121, v33, s63, v121
	v_pk_fma_f16 v26, v34, s96, v26
	v_pk_fma_f16 v27, v35, s97, v27
	v_pk_fma_f16 v28, v36, s98, v28
	v_pk_fma_f16 v29, v37, s99, v29
	s_waitcnt lgkmcnt(2)
	v_pk_fma_f16 v118, v106, s64, v118
	v_pk_fma_f16 v119, v107, s65, v119
	v_pk_fma_f16 v120, v108, s66, v120
	v_pk_fma_f16 v121, v109, s67, v121
	v_pk_fma_f16 v26, v110, s8, v26
	v_pk_fma_f16 v27, v111, s9, v27
	v_pk_fma_f16 v28, v112, s10, v28
	v_pk_fma_f16 v29, v113, s11, v29
	s_waitcnt lgkmcnt(0)
	v_pk_fma_f16 v26, v122, s12, v26
	v_pk_fma_f16 v27, v123, s13, v27
	v_pk_fma_f16 v28, v124, s14, v28
	v_pk_fma_f16 v29, v125, s15, v29
	v_pk_fma_f16 v109, v114, s68, v118
	v_pk_fma_f16 v123, v115, s69, v119
	v_pk_fma_f16 v122, v116, s70, v120
	v_pk_fma_f16 v105, v117, s71, v121
	v_mov_b64_e32 v[114:115], s[22:23]
	v_fma_mix_f32 v106, |v109|, s31, v104 op_sel_hi:[1,0,0]
	v_fma_mix_f32 v107, |v109|, s31, v104 op_sel:[1,0,0] op_sel_hi:[1,0,0]
	v_rcp_f32_e32 v106, v106
	v_rcp_f32_e32 v107, v107
	v_fma_mix_f32 v110, v109, s100, 0 op_sel_hi:[1,0,0]
	v_fma_mix_f32 v111, v109, s100, 0 op_sel:[1,0,0] op_sel_hi:[1,0,0]
	v_mul_f32_e64 v110, v110, -v110
	v_mul_f32_e64 v111, v111, -v111
	v_pk_fma_f32 v[116:117], v[106:107], s[24:25], v[114:115] op_sel_hi:[1,0,0]
	v_exp_f32_e32 v110, v110
	v_pk_fma_f32 v[116:117], v[116:117], v[106:107], s[26:27] op_sel_hi:[1,1,0]
	v_exp_f32_e32 v111, v111
	v_pk_fma_f32 v[116:117], v[116:117], v[106:107], s[28:29] op_sel_hi:[1,1,0]
	v_pk_max_f16 v112, v109, 0
	v_pk_fma_f32 v[116:117], v[116:117], v[106:107], s[30:31] op_sel_hi:[1,1,0]
	v_pk_mul_f32 v[106:107], v[106:107], v[116:117]
	v_pk_mul_f32 v[106:107], v[110:111], v[106:107]
	v_fma_mixlo_f16 v109, -|v109|, v106, v112 op_sel_hi:[1,0,1]
	v_fma_mixhi_f16 v109, -|v109|, v107, v112 op_sel:[1,0,1] op_sel_hi:[1,0,1]
	v_fma_mix_f32 v106, |v123|, s31, v104 op_sel_hi:[1,0,0]
	v_fma_mix_f32 v107, |v123|, s31, v104 op_sel:[1,0,0] op_sel_hi:[1,0,0]
	v_rcp_f32_e32 v106, v106
	v_rcp_f32_e32 v107, v107
	v_fma_mix_f32 v110, v123, s100, 0 op_sel_hi:[1,0,0]
	v_fma_mix_f32 v111, v123, s100, 0 op_sel:[1,0,0] op_sel_hi:[1,0,0]
	v_mul_f32_e64 v110, v110, -v110
	v_mul_f32_e64 v111, v111, -v111
	v_pk_fma_f32 v[116:117], v[106:107], s[24:25], v[114:115] op_sel_hi:[1,0,0]
	v_exp_f32_e32 v110, v110
	v_pk_fma_f32 v[116:117], v[116:117], v[106:107], s[26:27] op_sel_hi:[1,1,0]
	v_exp_f32_e32 v111, v111
	v_pk_fma_f32 v[116:117], v[116:117], v[106:107], s[28:29] op_sel_hi:[1,1,0]
	v_pk_max_f16 v112, v123, 0
	v_pk_fma_f32 v[116:117], v[116:117], v[106:107], s[30:31] op_sel_hi:[1,1,0]
	v_pk_mul_f32 v[106:107], v[106:107], v[116:117]
	v_pk_mul_f32 v[106:107], v[110:111], v[106:107]
	v_fma_mixlo_f16 v123, -|v123|, v106, v112 op_sel_hi:[1,0,1]
	v_fma_mixhi_f16 v123, -|v123|, v107, v112 op_sel:[1,0,1] op_sel_hi:[1,0,1]
	v_fma_mix_f32 v106, |v122|, s31, v104 op_sel_hi:[1,0,0]
	v_fma_mix_f32 v107, |v122|, s31, v104 op_sel:[1,0,0] op_sel_hi:[1,0,0]
	v_rcp_f32_e32 v106, v106
	v_rcp_f32_e32 v107, v107
	v_fma_mix_f32 v110, v122, s100, 0 op_sel_hi:[1,0,0]
	v_fma_mix_f32 v111, v122, s100, 0 op_sel:[1,0,0] op_sel_hi:[1,0,0]
	v_mul_f32_e64 v110, v110, -v110
	v_mul_f32_e64 v111, v111, -v111
	v_pk_fma_f32 v[116:117], v[106:107], s[24:25], v[114:115] op_sel_hi:[1,0,0]
	v_exp_f32_e32 v110, v110
	v_pk_fma_f32 v[116:117], v[116:117], v[106:107], s[26:27] op_sel_hi:[1,1,0]
	v_exp_f32_e32 v111, v111
	v_pk_fma_f32 v[116:117], v[116:117], v[106:107], s[28:29] op_sel_hi:[1,1,0]
	v_pk_max_f16 v112, v122, 0
	v_pk_fma_f32 v[116:117], v[116:117], v[106:107], s[30:31] op_sel_hi:[1,1,0]
	v_pk_mul_f32 v[106:107], v[106:107], v[116:117]
	v_pk_mul_f32 v[106:107], v[110:111], v[106:107]
	v_fma_mixlo_f16 v122, -|v122|, v106, v112 op_sel_hi:[1,0,1]
	v_fma_mixhi_f16 v122, -|v122|, v107, v112 op_sel:[1,0,1] op_sel_hi:[1,0,1]
	v_fma_mix_f32 v106, |v105|, s31, v104 op_sel_hi:[1,0,0]
	v_fma_mix_f32 v107, |v105|, s31, v104 op_sel:[1,0,0] op_sel_hi:[1,0,0]
	v_rcp_f32_e32 v106, v106
	v_rcp_f32_e32 v107, v107
	v_fma_mix_f32 v110, v105, s100, 0 op_sel_hi:[1,0,0]
	v_fma_mix_f32 v111, v105, s100, 0 op_sel:[1,0,0] op_sel_hi:[1,0,0]
	v_mul_f32_e64 v110, v110, -v110
	v_mul_f32_e64 v111, v111, -v111
	v_pk_fma_f32 v[116:117], v[106:107], s[24:25], v[114:115] op_sel_hi:[1,0,0]
	v_exp_f32_e32 v110, v110
	v_pk_fma_f32 v[116:117], v[116:117], v[106:107], s[26:27] op_sel_hi:[1,1,0]
	v_exp_f32_e32 v111, v111
	v_pk_fma_f32 v[116:117], v[116:117], v[106:107], s[28:29] op_sel_hi:[1,1,0]
	v_pk_max_f16 v112, v105, 0
	v_pk_fma_f32 v[116:117], v[116:117], v[106:107], s[30:31] op_sel_hi:[1,1,0]
	v_pk_mul_f32 v[106:107], v[106:107], v[116:117]
	v_pk_mul_f32 v[106:107], v[110:111], v[106:107]
	v_fma_mixlo_f16 v105, -|v105|, v106, v112 op_sel_hi:[1,0,1]
	v_fma_mixhi_f16 v105, -|v105|, v107, v112 op_sel:[1,0,1] op_sel_hi:[1,0,1]
	v_pk_mul_f16 v26, v26, v109
	v_pk_mul_f16 v27, v27, v123
	v_pk_mul_f16 v28, v28, v122
	s_nop 0
	v_pk_mul_f16 v29, v29, v105
	v_add_u32_e32 v30, s25, v78
	ds_write_b128 v30, v[26:29]
	s_waitcnt vmcnt(0)
	ds_write_b128 v39, v[22:25]
	s_and_saveexec_b64 s[32:33], s[4:5]
	s_cbranch_execz .LBB4_36
	ds_write_b128 v39, v[18:21] offset:8192
	s_branch .LBB4_36
